# code placement: everything from P1 on shifted by 4 bytes (one s_nop at the P1 entry): K-loop MFMA runs of P1/P8/P9/P11 on 8-byte phase 0
# speedup vs baseline: 1.0040x; 1.0040x over previous
; #define STAGGER(step_us) do { const unsigned long long _t0 = __builtin_amdgcn_s_memrealtime(), _d = (unsigned long long)(((bx >> 3) & 7) * (step_us) * (100.0f * STAGGER_SCALE)); \
;         while (__builtin_amdgcn_s_memrealtime() - _t0 < _d) __builtin_amdgcn_s_sleep(8); } while (0)
;     __host__ __device__ bool next(int i, Unit& u) const {
;         u.half = 0;
;         long L = (long)i * G + c;
;         if (tail > 0) { if (i > 0) return false; const int nt = nwg - tail * G; if (nt <= 0 || 2 * nt > G || c >= 2 * nt) return false; L = (long)tail * G + (c % nt); u.half = 1 + c / nt; }
;         else if (i >= rmax) return false;
;         if (L >= nwg) return false;
;         int wgid = (int)L; { const int q = nwg / NXCD, r = nwg % NXCD, xcd = wgid % NXCD, off = wgid / NXCD; wgid = (xcd < r ? xcd * (q + 1) : r * (q + 1) + (xcd - r) * q) + off; }
;         const int nig = wgm * nN, gid = wgid / nig, fm = gid * wgm, gsz = (nM - fm) < wgm ? (nM - fm) : wgm;
;         u.pm = pm0 + fm + ((wgid % nig) % gsz); u.pn = (wgid % nig) / gsz; return true;
; __global__ void __launch_bounds__(NWAVES * 64, 2) mk_fwd(Args args) {
;     ...
;     if (IN(1)) {
;         pg8::Gemm g{HB, (const bf16*)(ws + WS_WIN), M, INW, DM, DM}; pg8::StaticOrder S; S.init(M, INW, G, bx);
;         pg8::EpiProj E{PROJ, (const float*)(ws + WS_SSQ0), (const float*)(ws + WS_COS), (const float*)(ws + WS_SIN), P.sbq_norm, P.sbk_norm, (float*)(ws + WS_SSQSB)};
;         STAGGER(1.0f); pg8::gemm_phase<pg8::EpiProj, pg8::StaticOrder, true, true>(lds, g, S, E);
.LBB0_235:
	s_nop 0
	s_cmp_lt_i32 s74, 2
	s_cselect_b64 s[0:1], -1, 0
	s_add_u32 s42, s84, 0x26e00000
	s_addc_u32 s43, s85, 0
	s_and_b64 s[12:13], s[0:1], s[4:5]
	s_andn2_b64 vcc, exec, s[12:13]
	s_cbranch_vccnz .LBB0_342
	s_memrealtime s[0:1]
	s_waitcnt lgkmcnt(0)
	s_memrealtime s[0:1]
	s_cmpk_lt_i32 s2, 0xe00
	s_waitcnt lgkmcnt(0)
	s_cselect_b64 s[0:1], -1, 0
	s_cmpk_gt_i32 s2, 0xdff
	v_readfirstlane_b32 s6, v0
	s_cbranch_scc1 .LBB0_238
	s_ashr_i32 s3, s2, 31
	s_lshr_b32 s3, s3, 29
	s_add_i32 s3, s2, s3
	s_ashr_i32 s4, s3, 3
	s_and_b32 s3, s3, -8
	s_sub_i32 s3, s2, s3
	s_cmp_lt_i32 s3, 0
	s_movk_i32 s5, 0x1c1
	s_cselect_b32 s5, s5, 0x1c0
	s_mul_i32 s3, s3, s5
	s_add_i32 s3, s3, s4
	s_mul_hi_i32 s4, s3, 0x92492493
	s_add_i32 s4, s4, s3
	s_lshr_b32 s5, s4, 31
	s_ashr_i32 s4, s4, 8
	s_add_i32 s4, s4, s5
	s_lshl_b32 s5, s4, 3
	s_mulk_i32 s4, 0x1c0
	s_sub_i32 s3, s3, s4
	s_sext_i32_i16 s4, s3
	s_bfe_u32 s4, s4, 0x3001c
	s_add_i32 s4, s3, s4
	s_sext_i32_i16 s7, s4
	s_and_b32 s4, s4, 0xfff8
	s_sub_i32 s3, s3, s4
	s_sext_i32_i16 s3, s3
	s_add_i32 s8, s5, s3
	s_ashr_i32 s36, s7, 3
